# P10 down-GEMM LDS tile staged as full 128B lines (re-measure)
# speedup vs baseline: 1.0074x; 1.0074x over previous
; #define PG8_STAGE(bufoff, gbase, voff) do { _Pragma("unroll") for (int _i = 0; _i < 2; ++_i) { unsigned _vo = (voff)[_i]; asm volatile("" : "+v"(_vo)); \
;         __builtin_amdgcn_global_load_lds((const unsigned*)((const char*)(gbase) + _vo), (LAS unsigned*)(lds + (bufoff) + ldsw + _i * 8192), 16, 0, 0); } } while (0)
; #define PG8_STAGE_A(bufoff, gbase, h, go) do { if constexpr (Sched::GATHER) { PG8_STAGE(bufoff, gbase, go[h]); } else { PG8_STAGE(bufoff, (gbase) + (h) * hstep, voffA); } } while (0)
; #define PG8_WAIT_V(n) asm volatile("s_waitcnt vmcnt(" #n ")" ::: "memory")
; #define PG8_BAR __builtin_amdgcn_s_barrier()
;     ...
;     const int tid = threadIdx.x, wid = __builtin_amdgcn_readfirstlane(tid >> 6), lane = tid & 63, wr = wid >> 2, wc = wid & 3, fr = lane & 15, fq = lane >> 4;
;     const int nt = KB / 128;
;     unsigned voffA[2], voffB[2];
; #pragma unroll
;     for (int i = 0; i < 2; ++i) { int R, C; stage_rc(tid * 16 + i * 8192, R, C); const int Rb = Epi::PERM ? ((R & ~31) + perm32(R & 31)) : R;
;         voffA[i] = Sched::GATHER ? (unsigned)(C * 2) : (unsigned)(R * KB + C * 2); voffB[i] = (unsigned)(Rb * KB + C * 2); }
;     const size_t kstep = (size_t)(BK * 2);
;     const size_t hstep = (size_t)HALF * KB;
;     const unsigned ldsw = (unsigned)wid * 1024u;
;     const int aoff = lds_byte(wr * 64 + fr, fq * 8), boff = lds_byte(wc * 32 + fr, fq * 8);
;     ...
;     Unit cur, nxt; int ui = 0;
;     if (!S.next(0, cur)) return;
;     Acc acc;
; #pragma unroll
;     for (int a = 0; a < 2; ++a)
; #pragma unroll
;         for (int b = 0; b < 2; ++b)
; #pragma unroll
;             for (int m = 0; m < 4; ++m)
; #pragma unroll
;                 for (int n = 0; n < 2; ++n) acc[a][b][m][n] = (f32x4){0.f, 0.f, 0.f, 0.f};
;     bf16x8 At[4][2], B0[2][2], B1[2][2];
;     const char* cA = cur.a; const char* cB = cur.b;
;     unsigned gc[2][2], gn[2][2];
;     if constexpr (Sched::GATHER) { S.gather(cur, voffA, gc); }
;     if constexpr (Epi::PREF) E.prefetch(cur);
;     PG8_STAGE(PG8_SB(0, 0), cB, voffB); PG8_STAGE(PG8_SB(0, 1), cB + hstep, voffB); PG8_STAGE_A(PG8_SA(0, 0), cA, 0, gc); PG8_STAGE_A(PG8_SA(0, 1), cA, 1, gc);
;     if (wr == 1) PG8_BAR;
;     PG8_WAIT_V(2); PG8_BAR;
;     PG8_STAGE(PG8_SB(1, 0), cB + kstep, voffB); PG8_STAGE_A(PG8_SA(1, 0), cA + kstep, 0, gc); PG8_STAGE(PG8_SB(1, 1), cB + hstep + kstep, voffB);
;     PG8_WAIT_V(6); PG8_BAR;
.LBB5_1668:
	s_add_u32 s27, s22, 0x68000000
	s_addc_u32 s29, s23, 0
	v_lshrrev_b32_e32 v1, 4, v0
	v_xor_b32_e32 v1, v1, v0
	s_add_u32 s38, s22, 0x28000000
	v_and_b32_e32 v1, 7, v1
	s_addc_u32 s39, s23, 0
	s_lshr_b32 s11, s3, 21
	v_lshlrev_b32_e32 v3, 4, v1
	v_lshrrev_b32_e32 v6, 3, v0
	s_lshl_b32 s3, s11, 19
	v_and_b32_e32 v5, 0x23, v6
	v_and_b32_e32 v7, 12, v6
	s_add_u32 s18, s27, s3
	v_lshl_or_b32 v5, v7, 1, v5
	v_bfe_u32 v7, v6, 4, 1
	s_addc_u32 s19, s29, 0
	s_lshl_b32 s2, s2, 22
	s_lshl_b32 s3, s56, 19
	v_lshl_or_b32 v7, v7, 2, v5
	s_add_i32 s3, s3, s2
	v_lshl_or_b32 v1, v6, 11, v3
	v_or_b32_e32 v4, 64, v6
	s_add_u32 s34, s38, s3
	s_movk_i32 s2, 0x70
	s_addc_u32 s35, s39, 0
	s_movk_i32 s2, 0x60
	s_lshr_b32 s7, s8, 6
	v_lshl_or_b32 v140, v7, 11, v3
	v_or_b32_e32 v5, 64, v7
	s_lshl_b32 s40, s7, 10
	v_lshl_or_b32 v141, v4, 11, v3
	v_lshl_or_b32 v142, v5, 11, v3
	s_add_i32 s41, s40, 0
	v_mov_b32_e32 v3, v140
	s_add_i32 m0, s41, 0x10000
	s_lshr_b32 s6, s8, 8
	global_load_lds_dwordx4 v3, s[34:35]
	v_mov_b32_e32 v3, v142
	s_add_i32 m0, s41, 0x12000
	s_add_u32 s2, s34, 0x40000
	global_load_lds_dwordx4 v3, s[34:35]
	v_mov_b32_e32 v3, v140
	s_addc_u32 s3, s35, 0
	s_add_i32 m0, s41, 0x14000
	s_add_i32 s42, s41, 0x2000
	global_load_lds_dwordx4 v3, s[2:3]
	v_mov_b32_e32 v3, v142
	s_add_i32 m0, s41, 0x16000
	s_mov_b32 s57, 0
	global_load_lds_dwordx4 v3, s[2:3]
	v_mov_b32_e32 v3, v1
	s_mov_b32 m0, s41
	s_add_u32 s2, s18, 0x40000
	global_load_lds_dwordx4 v3, s[18:19]
	v_mov_b32_e32 v3, v141
	s_mov_b32 m0, s42
	s_addc_u32 s3, s19, 0
	global_load_lds_dwordx4 v3, s[18:19]
	s_add_i32 s43, s41, 0x4000
	v_mov_b32_e32 v3, v1
	s_mov_b32 m0, s43
	s_add_i32 s44, s41, 0x6000
	global_load_lds_dwordx4 v3, s[2:3]
	v_mov_b32_e32 v3, v141
	s_mov_b32 m0, s44
	s_cmp_eq_u32 s6, 1
	global_load_lds_dwordx4 v3, s[2:3]
	s_cselect_b64 s[2:3], -1, 0
	s_cmp_lg_u32 s6, 1
	s_cbranch_scc1 .LBB5_1670
	s_barrier
.LBB5_1670:
	s_add_u32 s4, s22, 0x8a000000
	s_addc_u32 s5, s23, 0
	s_lshl_b32 s45, s6, 6
	s_lshl_b32 s9, s6, 13
	s_lshl_b32 s6, s7, 5
	v_mov_b32_e32 v138, v140
	v_mov_b32_e32 v139, 0
	s_and_b32 s46, s6, 0x60
	s_waitcnt vmcnt(2)
	s_barrier
	s_mov_b64 s[6:7], 0x80
	v_lshl_add_u64 v[4:5], s[34:35], 0, v[138:139]
	s_add_i32 m0, s41, 0x18000
	v_lshl_add_u64 v[4:5], v[4:5], 0, s[6:7]
	v_mov_b32_e32 v138, v142
	global_load_lds_dwordx4 v[4:5], off
	s_add_i32 m0, s41, 0x1a000
	v_lshl_add_u64 v[4:5], s[34:35], 0, v[138:139]
	v_lshl_add_u64 v[4:5], v[4:5], 0, s[6:7]
	v_mov_b32_e32 v138, v1
	global_load_lds_dwordx4 v[4:5], off
	s_add_i32 s47, s41, 0x8000
	v_lshl_add_u64 v[4:5], s[18:19], 0, v[138:139]
	v_lshl_add_u64 v[4:5], v[4:5], 0, s[6:7]
	s_mov_b32 m0, s47
	v_mov_b32_e32 v138, v141
	s_lshl_b32 s10, s46, 7
	global_load_lds_dwordx4 v[4:5], off
	s_add_i32 s48, s41, 0xa000
	v_lshl_add_u64 v[4:5], s[18:19], 0, v[138:139]
	v_lshl_add_u64 v[4:5], v[4:5], 0, s[6:7]
	s_mov_b32 m0, s48
	s_add_u32 s12, s34, 0x40080
	v_mov_b32_e32 v3, v140
	global_load_lds_dwordx4 v[4:5], off
	s_addc_u32 s13, s35, 0
	s_add_i32 m0, s41, 0x1c000
	v_bfe_u32 v144, v0, 4, 2
	global_load_lds_dwordx4 v3, s[12:13]
	v_mov_b32_e32 v3, v142
	s_add_i32 m0, s41, 0x1e000
	v_and_b32_e32 v143, 15, v0
	global_load_lds_dwordx4 v3, s[12:13]
	v_lshrrev_b32_e32 v3, 1, v143
	v_xor_b32_e32 v3, v3, v144
	v_lshlrev_b32_e32 v3, 4, v3
	v_lshl_or_b32 v3, v143, 7, v3
	v_or_b32_e32 v4, s9, v3
	s_movk_i32 s9, 0x3c0
	s_cmpk_lt_u32 s8, 0x100
	v_or_b32_e32 v145, s10, v3
	s_waitcnt vmcnt(6)
	s_cselect_b64 s[8:9], -1, 0
	s_lshl_b32 s10, s46, 2
	s_add_i32 s49, s10, 0
	s_add_i32 s50, 0, 0x10000
	s_add_i32 s51, 0, 0x14000
	s_add_i32 s49, s49, 0x20800
	v_add_u32_e32 v146, s50, v145
	v_add_u32_e32 v147, s51, v145
	v_add_u32_e32 v148, 0, v4
	v_mov_b32_e32 v149, 0x7c7c7c7c
	v_lshlrev_b32_e32 v150, 2, v0
	s_mov_b32 s54, 0
	s_barrier
	s_branch .LBB5_1673

; #define PG8_STAGE(bufoff, gbase, voff) do { _Pragma("unroll") for (int _i = 0; _i < 2; ++_i) { unsigned _vo = (voff)[_i]; asm volatile("" : "+v"(_vo)); \
;         __builtin_amdgcn_global_load_lds((const unsigned*)((const char*)(gbase) + _vo), (LAS unsigned*)(lds + (bufoff) + ldsw + _i * 8192), 16, 0, 0); } } while (0)
; #define PG8_STAGE_A(bufoff, gbase, h, go) do { if constexpr (Sched::GATHER) { PG8_STAGE(bufoff, gbase, go[h]); } else { PG8_STAGE(bufoff, (gbase) + (h) * hstep, voffA); } } while (0)
; #define PG8_LDA(dst, b, h) do { _Pragma("unroll") for (int m = 0; m < 4; ++m) _Pragma("unroll") for (int k = 0; k < 2; ++k) dst[m][k] = *(const LAS bf16x8*)(lds + PG8_SA(b, h) + aoff + m * 2048 + k * 1024); } while (0)
; #define PG8_LDB(dst, b, h) do { _Pragma("unroll") for (int n = 0; n < 2; ++n) _Pragma("unroll") for (int k = 0; k < 2; ++k) dst[n][k] = *(const LAS bf16x8*)(lds + PG8_SB(b, h) + boff + n * 2048 + k * 1024); } while (0)
; #define PG8_WAIT_V(n) asm volatile("s_waitcnt vmcnt(" #n ")" ::: "memory")
; #define PG8_WAIT_L(n) asm volatile("s_waitcnt lgkmcnt(" #n ")" ::: "memory")
; #define PG8_BAR __builtin_amdgcn_s_barrier()
; #define PG8_SCHED __builtin_amdgcn_sched_barrier(0)
;     ...
;             const char* a1 = cA + (size_t)(t + 1) * kstep;
;             const char* a2 = last ? nA : cA + (size_t)(t + 2) * kstep; const char* b2 = last ? nB : cB + (size_t)(t + 2) * kstep;
;             const char* a3 = a2 + kstep; const char* b3 = b2 + kstep;
;             PG8_LDB(B0, 0, 0); PG8_LDB(B1, 0, 1); PG8_SCHED; PG8_LDA(At, 0, 0); PG8_STAGE_A(PG8_SA(1, 1), a1, 1, gc);
;             if constexpr (Sched::GATHER) { if (last) {
; #pragma unroll
;                 for (int h = 0; h < 2; ++h)
; #pragma unroll
;                     for (int i = 0; i < 2; ++i) gc[h][i] = gn[h][i]; } }
;             PG8_WAIT_V(8); PG8_WAIT_L(0); PG8_BAR; PG8_MMA(0, 0, At, B0); PG8_MMA(0, 1, At, B1); PG8_BAR; PG8_SCHED;
;             PG8_LDA(At, 0, 1); PG8_STAGE(PG8_SB(0, 0), b2, voffB); PG8_STAGE(PG8_SB(0, 1), b2 + hstep, voffB); PG8_STAGE_A(PG8_SA(0, 0), a2, 0, gc);
;             PG8_WAIT_V(8); PG8_WAIT_L(0); PG8_BAR; PG8_MMA(1, 0, At, B0); PG8_MMA(1, 1, At, B1); PG8_BAR; PG8_SCHED;
.LBB5_1678:
	ds_read_b128 v[130:133], v146
	ds_read_b128 v[152:155], v146 offset:2048
	v_xor_b32_e32 v146, 64, v146
	ds_read_b128 v[134:137], v146
	ds_read_b128 v[156:159], v146 offset:2048
	v_xor_b32_e32 v146, 64, v146
	ds_read_b128 v[160:163], v147
	ds_read_b128 v[168:171], v147 offset:2048
	v_xor_b32_e32 v147, 64, v147
	ds_read_b128 v[164:167], v147
	ds_read_b128 v[172:175], v147 offset:2048
	v_xor_b32_e32 v147, 64, v147
	s_add_u32 s34, s18, 0xfffc0080
	s_addc_u32 s35, s19, -1
	s_cmp_eq_u32 s64, 12
	s_cselect_b32 s35, s58, s35
	s_cselect_b32 s34, s59, s34
	s_cselect_b32 s37, s60, s63
	s_cselect_b32 s36, s61, s62
	v_mov_b32_e32 v138, v1
	ds_read_b128 v[176:179], v148
	ds_read_b128 v[184:187], v148 offset:2048
	ds_read_b128 v[200:203], v148 offset:4096
	ds_read_b128 v[208:211], v148 offset:6144
	v_xor_b32_e32 v148, 64, v148
	ds_read_b128 v[180:183], v148
	ds_read_b128 v[188:191], v148 offset:2048
	ds_read_b128 v[204:207], v148 offset:4096
	ds_read_b128 v[212:215], v148 offset:6144
	s_add_i32 m0, s41, 0xc000
	s_nop 0
	global_load_lds_dwordx4 v138, s[18:19]
	v_mov_b32_e32 v138, v141
	s_add_i32 m0, s41, 0xe000
	s_nop 0
	global_load_lds_dwordx4 v138, s[18:19]
	s_waitcnt vmcnt(8)
	s_waitcnt lgkmcnt(0)
	s_barrier
	s_setprio 1
	s_waitcnt lgkmcnt(0)
	v_mfma_scale_f32_16x16x128_f8f6f4 v[126:129], v[130:137], v[176:183], v[126:129], v149, v149 op_sel_hi:[0,0,0]
	v_mfma_scale_f32_16x16x128_f8f6f4 v[122:125], v[152:159], v[176:183], v[122:125], v149, v149 op_sel_hi:[0,0,0]
	v_mfma_scale_f32_16x16x128_f8f6f4 v[118:121], v[130:137], v[184:191], v[118:121], v149, v149 op_sel_hi:[0,0,0]
	v_mfma_scale_f32_16x16x128_f8f6f4 v[114:117], v[152:159], v[184:191], v[114:117], v149, v149 op_sel_hi:[0,0,0]
	v_mfma_scale_f32_16x16x128_f8f6f4 v[110:113], v[130:137], v[200:207], v[110:113], v149, v149 op_sel_hi:[0,0,0]
	v_mfma_scale_f32_16x16x128_f8f6f4 v[106:109], v[152:159], v[200:207], v[106:109], v149, v149 op_sel_hi:[0,0,0]
	v_mfma_scale_f32_16x16x128_f8f6f4 v[102:105], v[130:137], v[208:215], v[102:105], v149, v149 op_sel_hi:[0,0,0]
	v_mfma_scale_f32_16x16x128_f8f6f4 v[98:101], v[152:159], v[208:215], v[98:101], v149, v149 op_sel_hi:[0,0,0]
	s_setprio 0
	s_setprio 1
	v_mfma_scale_f32_16x16x128_f8f6f4 v[192:195], v[160:167], v[176:183], v[70:73], v149, v149 op_sel_hi:[0,0,0]
	v_mfma_scale_f32_16x16x128_f8f6f4 v[176:179], v[168:175], v[176:183], v[66:69], v149, v149 op_sel_hi:[0,0,0]
	v_mfma_scale_f32_16x16x128_f8f6f4 v[180:183], v[160:167], v[184:191], v[54:57], v149, v149 op_sel_hi:[0,0,0]
	v_mfma_scale_f32_16x16x128_f8f6f4 v[184:187], v[168:175], v[184:191], v[50:53], v149, v149 op_sel_hi:[0,0,0]
	v_mfma_scale_f32_16x16x128_f8f6f4 v[188:191], v[160:167], v[200:207], v[46:49], v149, v149 op_sel_hi:[0,0,0]
	v_mfma_scale_f32_16x16x128_f8f6f4 v[200:203], v[168:175], v[200:207], v[42:45], v149, v149 op_sel_hi:[0,0,0]
	v_mfma_scale_f32_16x16x128_f8f6f4 v[204:207], v[160:167], v[208:215], v[38:41], v149, v149 op_sel_hi:[0,0,0]
	v_mfma_scale_f32_16x16x128_f8f6f4 v[208:211], v[168:175], v[208:215], v[34:37], v149, v149 op_sel_hi:[0,0,0]
	s_setprio 0
	s_barrier
	v_mov_b32_e32 v138, v140
	s_add_i32 s65, s50, s40
	s_nop 2
	ds_read_b128 v[38:41], v148 offset:16384
	ds_read_b128 v[46:49], v148 offset:18432
	ds_read_b128 v[54:57], v148 offset:20480
	ds_read_b128 v[70:73], v148 offset:22528
	v_xor_b32_e32 v148, 64, v148
	ds_read_b128 v[34:37], v148 offset:16384
	ds_read_b128 v[42:45], v148 offset:18432
	ds_read_b128 v[50:53], v148 offset:20480
	ds_read_b128 v[66:69], v148 offset:22528
	s_mov_b32 m0, s65
	s_nop 0
	global_load_lds_dwordx4 v138, s[36:37]
	v_mov_b32_e32 v138, v142
	s_add_i32 m0, s65, 0x2000
	s_add_u32 s66, s36, 0x40000
	global_load_lds_dwordx4 v138, s[36:37]
	s_addc_u32 s67, s37, 0
	v_mov_b32_e32 v138, v140
	s_add_i32 s65, s51, s40
	s_mov_b32 m0, s65
	s_nop 0
	global_load_lds_dwordx4 v138, s[66:67]
	v_mov_b32_e32 v138, v142
	s_add_i32 m0, s65, 0x2000
	s_nop 0
	global_load_lds_dwordx4 v138, s[66:67]
	v_mov_b32_e32 v138, v1
	s_mov_b32 m0, s41
	s_nop 0
	global_load_lds_dwordx4 v138, s[34:35]
	v_mov_b32_e32 v138, v141
	s_mov_b32 m0, s42
	s_nop 0
	global_load_lds_dwordx4 v138, s[34:35]
	s_waitcnt vmcnt(8)
	s_waitcnt lgkmcnt(0)
	s_barrier
	s_setprio 1
	s_waitcnt lgkmcnt(0)
	v_mfma_scale_f32_16x16x128_f8f6f4 v[94:97], v[130:137], v[34:41], v[94:97], v149, v149 op_sel_hi:[0,0,0]
	v_mfma_scale_f32_16x16x128_f8f6f4 v[90:93], v[152:159], v[34:41], v[90:93], v149, v149 op_sel_hi:[0,0,0]
	v_mfma_scale_f32_16x16x128_f8f6f4 v[86:89], v[130:137], v[42:49], v[86:89], v149, v149 op_sel_hi:[0,0,0]
	v_mfma_scale_f32_16x16x128_f8f6f4 v[82:85], v[152:159], v[42:49], v[82:85], v149, v149 op_sel_hi:[0,0,0]
	v_mfma_scale_f32_16x16x128_f8f6f4 v[78:81], v[130:137], v[50:57], v[78:81], v149, v149 op_sel_hi:[0,0,0]
	v_mfma_scale_f32_16x16x128_f8f6f4 v[74:77], v[152:159], v[50:57], v[74:77], v149, v149 op_sel_hi:[0,0,0]
	v_mfma_scale_f32_16x16x128_f8f6f4 v[212:215], v[130:137], v[66:73], v[62:65], v149, v149 op_sel_hi:[0,0,0]
	v_mfma_scale_f32_16x16x128_f8f6f4 v[216:219], v[152:159], v[66:73], v[58:61], v149, v149 op_sel_hi:[0,0,0]
	s_setprio 0
	s_setprio 1
	v_mfma_scale_f32_16x16x128_f8f6f4 v[220:223], v[160:167], v[34:41], v[30:33], v149, v149 op_sel_hi:[0,0,0]
	v_mfma_scale_f32_16x16x128_f8f6f4 v[224:227], v[168:175], v[34:41], v[26:29], v149, v149 op_sel_hi:[0,0,0]
	v_mfma_scale_f32_16x16x128_f8f6f4 v[228:231], v[160:167], v[42:49], v[22:25], v149, v149 op_sel_hi:[0,0,0]
	v_mfma_scale_f32_16x16x128_f8f6f4 v[232:235], v[168:175], v[42:49], v[18:21], v149, v149 op_sel_hi:[0,0,0]
	v_mfma_scale_f32_16x16x128_f8f6f4 v[236:239], v[160:167], v[50:57], v[14:17], v149, v149 op_sel_hi:[0,0,0]
	v_mfma_scale_f32_16x16x128_f8f6f4 v[240:243], v[168:175], v[50:57], v[10:13], v149, v149 op_sel_hi:[0,0,0]
	v_mfma_scale_f32_16x16x128_f8f6f4 v[244:247], v[160:167], v[66:73], v[6:9], v149, v149 op_sel_hi:[0,0,0]
	v_mfma_scale_f32_16x16x128_f8f6f4 v[248:251], v[168:175], v[66:73], v[2:5], v149, v149 op_sel_hi:[0,0,0]
	s_setprio 0
	s_barrier
; #define PG8_STAGE(bufoff, gbase, voff) do { _Pragma("unroll") for (int _i = 0; _i < 2; ++_i) { unsigned _vo = (voff)[_i]; asm volatile("" : "+v"(_vo)); \
;         __builtin_amdgcn_global_load_lds((const unsigned*)((const char*)(gbase) + _vo), (LAS unsigned*)(lds + (bufoff) + ldsw + _i * 8192), 16, 0, 0); } } while (0)
; #define PG8_STAGE_A(bufoff, gbase, h, go) do { if constexpr (Sched::GATHER) { PG8_STAGE(bufoff, gbase, go[h]); } else { PG8_STAGE(bufoff, (gbase) + (h) * hstep, voffA); } } while (0)
; #define PG8_LDA(dst, b, h) do { _Pragma("unroll") for (int m = 0; m < 4; ++m) _Pragma("unroll") for (int k = 0; k < 2; ++k) dst[m][k] = *(const LAS bf16x8*)(lds + PG8_SA(b, h) + aoff + m * 2048 + k * 1024); } while (0)
; #define PG8_LDB(dst, b, h) do { _Pragma("unroll") for (int n = 0; n < 2; ++n) _Pragma("unroll") for (int k = 0; k < 2; ++k) dst[n][k] = *(const LAS bf16x8*)(lds + PG8_SB(b, h) + boff + n * 2048 + k * 1024); } while (0)
; #define PG8_WAIT_V(n) asm volatile("s_waitcnt vmcnt(" #n ")" ::: "memory")
; #define PG8_WAIT_L(n) asm volatile("s_waitcnt lgkmcnt(" #n ")" ::: "memory")
; #define PG8_BAR __builtin_amdgcn_s_barrier()
; #define PG8_SCHED __builtin_amdgcn_sched_barrier(0)
;     ...
;             PG8_LDB(B0, 1, 0); PG8_LDB(B1, 1, 1); PG8_SCHED; PG8_LDA(At, 1, 0); PG8_STAGE_A(PG8_SA(0, 1), a2, 1, gc);
;             PG8_WAIT_V(8); PG8_WAIT_L(0); PG8_BAR; PG8_MMA(0, 0, At, B0); PG8_MMA(0, 1, At, B1); PG8_BAR; PG8_SCHED;
;             PG8_LDA(At, 1, 1); PG8_STAGE(PG8_SB(1, 0), b3, voffB); PG8_STAGE(PG8_SB(1, 1), b3 + hstep, voffB); PG8_STAGE_A(PG8_SA(1, 0), a3, 0, gc);
;             PG8_WAIT_V(8); PG8_WAIT_L(0); PG8_BAR; PG8_MMA(1, 0, At, B0); PG8_MMA(1, 1, At, B1); PG8_BAR; PG8_SCHED;
;         }
	s_add_i32 s65, 0, 0x18000
	s_add_i32 s68, 0, 0x1c000
	v_add_u32_e32 v14, s65, v145
	v_add_u32_e32 v18, s68, v145
	s_nop 0
	ds_read_b128 v[2:5], v14
	ds_read_b128 v[10:13], v14 offset:2048
	v_xor_b32_e32 v14, 64, v14
	ds_read_b128 v[6:9], v14
	ds_read_b128 v[14:17], v14 offset:2048
	ds_read_b128 v[130:133], v18
	ds_read_b128 v[152:155], v18 offset:2048
	v_xor_b32_e32 v18, 64, v18
	ds_read_b128 v[134:137], v18
	ds_read_b128 v[156:159], v18 offset:2048
	s_add_u32 s66, s34, 0x40000
	v_mov_b32_e32 v42, v1
	s_mov_b32 m0, s43
	ds_read_b128 v[18:21], v148 offset:32768
	ds_read_b128 v[26:29], v148 offset:34816
	ds_read_b128 v[34:37], v148 offset:36864
	ds_read_b128 v[58:61], v148 offset:38912
	v_xor_b32_e32 v148, 64, v148
	ds_read_b128 v[22:25], v148 offset:32768
	ds_read_b128 v[30:33], v148 offset:34816
	ds_read_b128 v[38:41], v148 offset:36864
	ds_read_b128 v[62:65], v148 offset:38912
	s_addc_u32 s67, s35, 0
	s_nop 0
	global_load_lds_dwordx4 v42, s[66:67]
	v_mov_b32_e32 v42, v141
	s_mov_b32 m0, s44
	s_nop 0
	global_load_lds_dwordx4 v42, s[66:67]
	s_waitcnt vmcnt(8)
	s_waitcnt lgkmcnt(0)
	s_barrier
	s_setprio 1
	s_waitcnt lgkmcnt(0)
	v_mfma_scale_f32_16x16x128_f8f6f4 v[126:129], v[2:9], v[18:25], v[126:129], v149, v149 op_sel_hi:[0,0,0]
	v_mfma_scale_f32_16x16x128_f8f6f4 v[122:125], v[10:17], v[18:25], v[122:125], v149, v149 op_sel_hi:[0,0,0]
	v_mfma_scale_f32_16x16x128_f8f6f4 v[118:121], v[2:9], v[26:33], v[118:121], v149, v149 op_sel_hi:[0,0,0]
	v_mfma_scale_f32_16x16x128_f8f6f4 v[114:117], v[10:17], v[26:33], v[114:117], v149, v149 op_sel_hi:[0,0,0]
	v_mfma_scale_f32_16x16x128_f8f6f4 v[110:113], v[2:9], v[34:41], v[110:113], v149, v149 op_sel_hi:[0,0,0]
	v_mfma_scale_f32_16x16x128_f8f6f4 v[106:109], v[10:17], v[34:41], v[106:109], v149, v149 op_sel_hi:[0,0,0]
	v_mfma_scale_f32_16x16x128_f8f6f4 v[102:105], v[2:9], v[58:65], v[102:105], v149, v149 op_sel_hi:[0,0,0]
	v_mfma_scale_f32_16x16x128_f8f6f4 v[98:101], v[10:17], v[58:65], v[98:101], v149, v149 op_sel_hi:[0,0,0]
	s_setprio 0
	s_setprio 1
	v_mfma_scale_f32_16x16x128_f8f6f4 v[70:73], v[130:137], v[18:25], v[192:195], v149, v149 op_sel_hi:[0,0,0]
	v_mfma_scale_f32_16x16x128_f8f6f4 v[66:69], v[152:159], v[18:25], v[176:179], v149, v149 op_sel_hi:[0,0,0]
	v_mfma_scale_f32_16x16x128_f8f6f4 v[54:57], v[130:137], v[26:33], v[180:183], v149, v149 op_sel_hi:[0,0,0]
	v_mfma_scale_f32_16x16x128_f8f6f4 v[50:53], v[152:159], v[26:33], v[184:187], v149, v149 op_sel_hi:[0,0,0]
	v_mfma_scale_f32_16x16x128_f8f6f4 v[46:49], v[130:137], v[34:41], v[188:191], v149, v149 op_sel_hi:[0,0,0]
	v_mfma_scale_f32_16x16x128_f8f6f4 v[42:45], v[152:159], v[34:41], v[200:203], v149, v149 op_sel_hi:[0,0,0]
	v_mfma_scale_f32_16x16x128_f8f6f4 v[38:41], v[130:137], v[58:65], v[204:207], v149, v149 op_sel_hi:[0,0,0]
	v_mfma_scale_f32_16x16x128_f8f6f4 v[34:37], v[152:159], v[58:65], v[208:211], v149, v149 op_sel_hi:[0,0,0]
	s_setprio 0
	s_barrier
	v_mov_b32_e32 v138, v140
	ds_read_b128 v[22:25], v148 offset:49152
	ds_read_b128 v[164:167], v148 offset:51200
	ds_read_b128 v[172:175], v148 offset:53248
	ds_read_b128 v[180:183], v148 offset:55296
	v_xor_b32_e32 v148, 64, v148
	ds_read_b128 v[18:21], v148 offset:49152
	ds_read_b128 v[160:163], v148 offset:51200
	ds_read_b128 v[168:171], v148 offset:53248
	ds_read_b128 v[176:179], v148 offset:55296
	s_add_i32 s65, s65, s40
	v_lshl_add_u64 v[26:27], s[36:37], 0, v[138:139]
	v_lshl_add_u64 v[26:27], v[26:27], 0, s[6:7]
	s_mov_b32 m0, s65
	v_mov_b32_e32 v138, v142
	global_load_lds_dwordx4 v[26:27], off
	s_add_i32 m0, s65, 0x2000
	v_lshl_add_u64 v[26:27], s[36:37], 0, v[138:139]
	v_lshl_add_u64 v[26:27], v[26:27], 0, s[6:7]
	s_add_u32 s36, s36, 0x40080
	global_load_lds_dwordx4 v[26:27], off
	s_addc_u32 s37, s37, 0
	v_mov_b32_e32 v26, v140
	s_add_i32 s65, s68, s40
	s_mov_b32 m0, s65
	v_mov_b32_e32 v138, v1
	global_load_lds_dwordx4 v26, s[36:37]
	v_mov_b32_e32 v26, v142
	s_add_i32 m0, s65, 0x2000
	s_nop 0
	global_load_lds_dwordx4 v26, s[36:37]
	s_mov_b32 m0, s47
	v_lshl_add_u64 v[26:27], s[34:35], 0, v[138:139]
	v_lshl_add_u64 v[26:27], v[26:27], 0, s[6:7]
	v_mov_b32_e32 v138, v141
	global_load_lds_dwordx4 v[26:27], off
	s_mov_b32 m0, s48
	v_lshl_add_u64 v[26:27], s[34:35], 0, v[138:139]
	v_lshl_add_u64 v[26:27], v[26:27], 0, s[6:7]
	global_load_lds_dwordx4 v[26:27], off
	s_waitcnt vmcnt(8)
	s_waitcnt lgkmcnt(0)
	s_barrier
	s_setprio 1
	s_waitcnt lgkmcnt(0)
	v_mfma_scale_f32_16x16x128_f8f6f4 v[94:97], v[2:9], v[18:25], v[94:97], v149, v149 op_sel_hi:[0,0,0]
	v_mfma_scale_f32_16x16x128_f8f6f4 v[90:93], v[10:17], v[18:25], v[90:93], v149, v149 op_sel_hi:[0,0,0]
	v_mfma_scale_f32_16x16x128_f8f6f4 v[86:89], v[2:9], v[160:167], v[86:89], v149, v149 op_sel_hi:[0,0,0]
	v_mfma_scale_f32_16x16x128_f8f6f4 v[82:85], v[10:17], v[160:167], v[82:85], v149, v149 op_sel_hi:[0,0,0]
	v_mfma_scale_f32_16x16x128_f8f6f4 v[78:81], v[2:9], v[168:175], v[78:81], v149, v149 op_sel_hi:[0,0,0]
	v_mfma_scale_f32_16x16x128_f8f6f4 v[74:77], v[10:17], v[168:175], v[74:77], v149, v149 op_sel_hi:[0,0,0]
	v_mfma_scale_f32_16x16x128_f8f6f4 v[62:65], v[2:9], v[176:183], v[212:215], v149, v149 op_sel_hi:[0,0,0]
	v_mfma_scale_f32_16x16x128_f8f6f4 v[58:61], v[10:17], v[176:183], v[216:219], v149, v149 op_sel_hi:[0,0,0]
	s_setprio 0
	s_setprio 1
	v_mfma_scale_f32_16x16x128_f8f6f4 v[30:33], v[130:137], v[18:25], v[220:223], v149, v149 op_sel_hi:[0,0,0]
	v_mfma_scale_f32_16x16x128_f8f6f4 v[26:29], v[152:159], v[18:25], v[224:227], v149, v149 op_sel_hi:[0,0,0]
	v_mfma_scale_f32_16x16x128_f8f6f4 v[22:25], v[130:137], v[160:167], v[228:231], v149, v149 op_sel_hi:[0,0,0]
	v_mfma_scale_f32_16x16x128_f8f6f4 v[18:21], v[152:159], v[160:167], v[232:235], v149, v149 op_sel_hi:[0,0,0]
	v_mfma_scale_f32_16x16x128_f8f6f4 v[14:17], v[130:137], v[168:175], v[236:239], v149, v149 op_sel_hi:[0,0,0]
	v_mfma_scale_f32_16x16x128_f8f6f4 v[10:13], v[152:159], v[168:175], v[240:243], v149, v149 op_sel_hi:[0,0,0]
	v_mfma_scale_f32_16x16x128_f8f6f4 v[6:9], v[130:137], v[176:183], v[244:247], v149, v149 op_sel_hi:[0,0,0]
	v_mfma_scale_f32_16x16x128_f8f6f4 v[2:5], v[152:159], v[176:183], v[248:251], v149, v149 op_sel_hi:[0,0,0]
	s_setprio 0
	s_barrier
	s_add_i32 s64, s64, 2
	s_add_u32 s18, s18, 0x100
	s_addc_u32 s19, s19, 0
	s_add_u32 s62, s62, 0x100
	s_addc_u32 s63, s63, 0
	s_cmp_gt_u32 s64, 13
	s_cbranch_scc0 .LBB5_1678
	s_and_b64 vcc, exec, s[8:9]
	s_cbranch_vccz .LBB5_1681
	s_barrier
